# speedup vs baseline: 1.0182x; 1.0182x over previous
.Lk2f_b2:
	s_waitcnt lgkmcnt(0)
	s_barrier
	v_and_b32_e32 v1, 63, v0
	v_lshlrev_b32_e32 v6, 3, v1
	ds_read_b64 v[14:15], v6 offset:18688
	s_cmp_eq_u32 s4, 7
	s_cbranch_scc1 .Lk2f_w7
	v_lshrrev_b32_e32 v3, 2, v1
	s_mul_i32 s5, s4, 14
	v_add_u32_e32 v6, s5, v3
	v_cmp_gt_u32_e32 vcc, 14, v3
	v_mov_b32_e32 v7, 0x7f
	v_mov_b32_e32 v8, 0x62
	v_and_b32_e32 v9, 3, v1
	v_cndmask_b32_e32 v7, v7, v6, vcc
	v_cndmask_b32_e32 v8, v8, v6, vcc
	v_lshlrev_b32_e32 v7, 2, v7
	v_mul_u32_u24_e32 v2, 0x90, v8
	ds_read_b32 v3, v7 offset:18688
	ds_read_b128 v[4:7], v2 offset:19456
	v_lshlrev_b32_e32 v1, 4, v9
	s_mov_b32 s32, s8
	s_and_b32 s33, s9, 0xffff
	s_mov_b32 s34, 0xc35000
	s_mov_b32 s35, 0x20000
	v_and_b32_e32 v8, 15, v0
	v_add_u32_e32 v9, s5, v8
	s_mul_i32 s6, s3, 0x62
	v_add_u32_e32 v9, s6, v9
	v_cmp_gt_u32_e32 vcc, 14, v8
	s_mov_b32 s7, 0x186a0
	v_cmp_gt_u32_e64 s[38:39], s7, v9
	s_and_b64 vcc, vcc, s[38:39]
	s_mov_b64 s[40:41], vcc
	v_and_b32_e32 v8, 0x30, v0
	v_cndmask_b32_e32 v9, 0, v9, vcc
	v_lshl_or_b32 v8, v9, 7, v8
	buffer_load_dwordx4 v[56:59], v8, s[32:35], 0 offen
	buffer_load_dwordx4 v[60:63], v8, s[32:35], 0 offen offset:64
	v_mov_b32_e32 v40, 0
	v_mov_b32_e32 v41, 0
	v_mov_b32_e32 v42, 0
	v_mov_b32_e32 v43, 0
	v_mov_b32_e32 v44, 0
	v_mov_b32_e32 v45, 0
	v_mov_b32_e32 v46, 0
	v_mov_b32_e32 v47, 0
	v_mov_b32_e32 v48, 0
	v_mov_b32_e32 v49, 0
	v_mov_b32_e32 v50, 0
	v_mov_b32_e32 v51, 0
	v_mov_b32_e32 v52, 0
	v_mov_b32_e32 v53, 0
	v_mov_b32_e32 v54, 0
	v_mov_b32_e32 v55, 0
	s_mov_b32 s5, 0
	s_waitcnt lgkmcnt(0)
	v_max_u32_e32 v8, v14, v15
	v_cmp_lt_u32_e32 vcc, 32, v8
	s_cmp_lg_u64 vcc, 0
	s_cbranch_scc1 .Lk2f_fallback
	v_cmp_lt_u32_e32 vcc, 16, v3
	s_mov_b64 s[52:53], 0
	s_cmp_lg_u64 vcc, 0
	s_cbranch_scc0 .Lk2f_nosplit
	s_mov_b64 s[44:45], vcc
	s_ff1_i32_b64 s6, s[44:45]
	s_lshl_b64 s[46:47], 15, s6
	s_andn2_b64 s[44:45], s[44:45], s[46:47]
	s_mov_b64 s[50:51], 0
	s_cmp_lg_u64 s[44:45], 0
	s_cbranch_scc0 .Lk2f_sp1
	s_ff1_i32_b64 s7, s[44:45]
	s_lshl_b64 s[50:51], 15, s7
	s_andn2_b64 s[44:45], s[44:45], s[50:51]
	s_cmp_lg_u64 s[44:45], 0
	s_cbranch_scc1 .Lk2f_nosplit
.Lk2f_sp1:
	v_readlane_b32 s38, v3, s6
	v_readlane_b32 s39, v2, s6
	s_or_b64 s[52:53], s[46:47], s[50:51]
	s_sub_i32 s38, s38, 16
	s_add_i32 s39, s39, 64
	v_mov_b32_e32 v8, s38
	v_mov_b32_e32 v9, s39
	v_mov_b32_e32 v10, 16
	s_mov_b32 s48, 0
	s_mov_b32 s49, 0xf000000
	v_cndmask_b32_e64 v3, v3, v8, s[48:49]
	v_cndmask_b32_e64 v2, v2, v9, s[48:49]
	s_cmp_lg_u64 s[50:51], 0
	s_cbranch_scc0 .Lk2f_sp2
	v_readlane_b32 s38, v3, s7
	v_readlane_b32 s39, v2, s7
	s_mov_b32 s49, 0xf0000000
	s_sub_i32 s38, s38, 16
	s_add_i32 s39, s39, 64
	v_mov_b32_e32 v8, s38
	v_mov_b32_e32 v9, s39
	s_nop 0
	v_cndmask_b32_e64 v3, v3, v8, s[48:49]
	v_cndmask_b32_e64 v2, v2, v9, s[48:49]
.Lk2f_sp2:
	v_cndmask_b32_e64 v3, v3, v10, s[52:53]
	ds_read_b128 v[4:7], v2 offset:19456
	s_waitcnt lgkmcnt(0)
.Lk2f_nosplit:
	v_cmp_lt_i32_e32 vcc, 0, v3
	s_cmp_lg_u64 vcc, 0
	s_cbranch_scc0 .Lk2f_gdone

.Lk2f_gdone:
	s_cmp_lg_u64 s[52:53], 0
	s_cbranch_scc0 .Lk2f_nocomb
	v_and_b32_e32 v8, 63, v0
	v_and_b32_e32 v9, 3, v8
	v_add_u32_e32 v10, 56, v9
	v_add_u32_e32 v11, 60, v9
	s_ff1_i32_b64 s6, s[52:53]
	s_lshl_b64 s[46:47], 15, s6
	s_andn2_b64 s[48:49], s[52:53], s[46:47]
	v_cndmask_b32_e64 v8, v8, v10, s[46:47]
	v_cndmask_b32_e64 v8, v8, v11, s[48:49]
	v_lshlrev_b32_e32 v8, 2, v8
	ds_bpermute_b32 v12, v8, v3
	ds_bpermute_b32 v16, v8, v40
	ds_bpermute_b32 v17, v8, v41
	ds_bpermute_b32 v18, v8, v42
	ds_bpermute_b32 v19, v8, v43
	ds_bpermute_b32 v20, v8, v44
	ds_bpermute_b32 v21, v8, v45
	ds_bpermute_b32 v22, v8, v46
	ds_bpermute_b32 v23, v8, v47
	s_waitcnt lgkmcnt(0)
	ds_bpermute_b32 v24, v8, v48
	ds_bpermute_b32 v25, v8, v49
	ds_bpermute_b32 v26, v8, v50
	ds_bpermute_b32 v27, v8, v51
	ds_bpermute_b32 v28, v8, v52
	ds_bpermute_b32 v29, v8, v53
	ds_bpermute_b32 v30, v8, v54
	ds_bpermute_b32 v31, v8, v55
	s_mov_b64 exec, s[52:53]
	v_add_u32_e32 v3, v3, v12
	v_add_f32_e32 v40, v40, v16
	v_add_f32_e32 v41, v41, v17
	v_add_f32_e32 v42, v42, v18
	v_add_f32_e32 v43, v43, v19
	v_add_f32_e32 v44, v44, v20
	v_add_f32_e32 v45, v45, v21
	v_add_f32_e32 v46, v46, v22
	v_add_f32_e32 v47, v47, v23
	s_waitcnt lgkmcnt(0)
	v_add_f32_e32 v48, v48, v24
	v_add_f32_e32 v49, v49, v25
	v_add_f32_e32 v50, v50, v26
	v_add_f32_e32 v51, v51, v27
	v_add_f32_e32 v52, v52, v28
	v_add_f32_e32 v53, v53, v29
	v_add_f32_e32 v54, v54, v30
	v_add_f32_e32 v55, v55, v31
	s_mov_b64 exec, -1
